# MoE GEMM tile heads: tile->expert entry via scalar load (no vmcnt(0) drain of epilogue stores at each tile boundary)
# baseline (speedup 1.0000x reference)
;     __device__ bool next(int i, Unit& u) const { if (i > 0 || c >= 16) return false; u.pm = c; u.pn = 0; u.be = c >> 3; return true; }
;     __device__ bool next(int i, Unit& u) const {
;         const long L = (long)i * G + c; if (L >= nwg) return false;
;         static_map((int)L, nM, nN, u.pm, u.pn); u.be = __builtin_amdgcn_readfirstlane(tile_e[u.pm]); return true;
;     }
.LBB0_1094:
	s_add_i32 s54, s54, 1
	v_readlane_b32 s0, v252, 38
	v_readlane_b32 s4, v252, 37
	s_mul_i32 s0, s54, s0
	s_mul_hi_u32 s1, s54, s4
	s_add_i32 s1, s1, s0
	s_mul_i32 s0, s54, s4
	v_readlane_b32 s4, v254, 40
	v_readlane_b32 s5, v254, 41
	s_add_u32 s0, s0, s4
	s_addc_u32 s1, s1, s5
	v_mov_b64_e32 v[2:3], s[6:7]
	v_cmp_ge_i64_e32 vcc, s[0:1], v[2:3]
	v_cmp_lt_i64_e64 s[4:5], s[0:1], v[2:3]
	s_mov_b64 s[20:21], s[10:11]
	s_cbranch_vccnz .LBB0_1096
	s_ashr_i32 s1, s0, 31
	s_lshr_b32 s1, s1, 29
	s_add_i32 s1, s0, s1
	s_ashr_i32 s14, s1, 3
	s_and_b32 s1, s1, -8
	s_sub_i32 s0, s0, s1
	s_cmp_lt_i32 s0, 0
	s_cselect_b32 s1, s49, s48
	s_mul_i32 s0, s0, s1
	s_add_i32 s0, s0, s14
	s_mul_hi_i32 s1, s0, 0x92492493
	s_add_i32 s1, s1, s0
	s_lshr_b32 s14, s1, 31
	s_ashr_i32 s1, s1, 8
	s_add_i32 s1, s1, s14
	s_lshl_b32 s14, s1, 3
	s_sub_i32 s15, s28, s14
	s_min_i32 s15, s15, 8
	s_abs_i32 s16, s15
	v_cvt_f32_u32_e32 v2, s16
	s_sub_i32 s18, 0, s16
	s_mulk_i32 s1, 0x1c0
	s_sub_i32 s0, s0, s1
	v_rcp_iflag_f32_e32 v2, v2
	s_abs_i32 s1, s0
	s_xor_b32 s17, s0, s15
	s_ashr_i32 s17, s17, 31
	v_mul_f32_e32 v2, 0x4f7ffffe, v2
	v_cvt_u32_f32_e32 v2, v2
	s_nop 0
	v_readfirstlane_b32 s19, v2
	s_mul_i32 s18, s18, s19
	s_mul_hi_u32 s18, s19, s18
	s_add_i32 s19, s19, s18
	s_mul_hi_u32 s18, s1, s19
	s_mul_i32 s19, s18, s16
	s_sub_i32 s1, s1, s19
	s_add_i32 s20, s18, 1
	s_sub_i32 s19, s1, s16
	s_cmp_ge_u32 s1, s16
	s_cselect_b32 s18, s20, s18
	s_cselect_b32 s1, s19, s1
	s_add_i32 s19, s18, 1
	s_cmp_ge_u32 s1, s16
	s_cselect_b32 s1, s19, s18
	s_xor_b32 s1, s1, s17
	s_sub_i32 s16, s1, s17
	s_mul_i32 s1, s16, s15
	s_sub_i32 s0, s0, s1
	s_add_i32 s18, s14, s0
	s_ashr_i32 s19, s18, 31
	s_lshl_b64 s[0:1], s[18:19], 2
	v_readlane_b32 s14, v252, 25
	s_add_u32 s0, s14, s0
	v_readlane_b32 s14, v252, 26
	s_addc_u32 s1, s14, s1
	s_load_dword s55, s[0:1], 0x0 glc
	s_mov_b64 s[20:21], -1
	s_waitcnt lgkmcnt(0)

;     __device__ bool next(int i, Unit& u) const { if (i > 0 || c >= 16) return false; u.pm = c; u.pn = 0; u.be = c >> 3; return true; }
;     __device__ bool next(int i, Unit& u) const {
;         const long L = (long)i * G + c; if (L >= nwg) return false;
;         int v, pn; static_map((int)L, nV, nN, v, pn); const int h = v >= nT ? 1 : 0, t = v - h * nT;
;         u.pm = h * MAXPT + t; u.pn = pn; u.be = __builtin_amdgcn_readfirstlane(tile_e[t]) * 2 + h; return true;
;     }
.LBB0_1255:
	s_add_i32 s50, s50, 1
	v_readlane_b32 s0, v252, 10
	s_mul_i32 s0, s50, s0
	s_mul_hi_u32 s1, s50, s33
	s_add_i32 s1, s1, s0
	s_mul_i32 s0, s50, s33
	v_readlane_b32 s4, v254, 40
	v_readlane_b32 s5, v254, 41
	s_add_u32 s0, s0, s4
	s_addc_u32 s1, s1, s5
	v_mov_b64_e32 v[2:3], s[6:7]
	v_cmp_ge_i64_e32 vcc, s[0:1], v[2:3]
	v_cmp_lt_i64_e64 s[4:5], s[0:1], v[2:3]
	s_cbranch_vccnz .LBB0_1257
	s_ashr_i32 s1, s0, 31
	s_lshr_b32 s1, s1, 29
	s_add_i32 s1, s0, s1
	s_ashr_i32 s12, s1, 3
	s_and_b32 s1, s1, -8
	s_sub_i32 s0, s0, s1
	s_cmp_lt_i32 s0, 0
	s_cselect_b32 s1, s41, s31
	s_mul_i32 s0, s0, s1
	s_add_i32 s0, s0, s12
	s_ashr_i32 s1, s0, 31
	s_lshr_b32 s1, s1, 26
	s_add_i32 s1, s0, s1
	s_ashr_i32 s12, s1, 6
	s_lshl_b32 s12, s12, 3
	s_sub_i32 s13, s31, s12
	s_min_i32 s13, s13, 8
	s_abs_i32 s14, s13
	v_cvt_f32_u32_e32 v2, s14
	s_sub_i32 s20, 0, s14
	s_andn2_b32 s1, s1, 63
	s_sub_i32 s0, s0, s1
	v_rcp_iflag_f32_e32 v2, v2
	s_abs_i32 s1, s0
	s_xor_b32 s15, s0, s13
	s_ashr_i32 s15, s15, 31
	v_mul_f32_e32 v2, 0x4f7ffffe, v2
	v_cvt_u32_f32_e32 v2, v2
	s_nop 0
	v_readfirstlane_b32 s21, v2
	s_mul_i32 s20, s20, s21
	s_mul_hi_u32 s20, s21, s20
	s_add_i32 s21, s21, s20
	s_mul_hi_u32 s20, s1, s21
	s_mul_i32 s21, s20, s14
	s_sub_i32 s1, s1, s21
	s_add_i32 s22, s20, 1
	s_sub_i32 s21, s1, s14
	s_cmp_ge_u32 s1, s14
	s_cselect_b32 s20, s22, s20
	s_cselect_b32 s1, s21, s1
	s_add_i32 s21, s20, 1
	s_cmp_ge_u32 s1, s14
	s_cselect_b32 s1, s21, s20
	s_xor_b32 s1, s1, s15
	s_sub_i32 s51, s1, s15
	s_mul_i32 s1, s51, s13
	s_sub_i32 s0, s0, s1
	s_add_i32 s12, s12, s0
	s_cmp_ge_i32 s12, s28
	s_cselect_b64 s[0:1], -1, 0
	v_cndmask_b32_e64 v2, 0, 1, s[0:1]
	s_and_b64 s[0:1], s[0:1], exec
	s_cselect_b32 s0, s28, 0
	s_cselect_b32 s1, 0x48, 0
	s_sub_i32 s0, s12, s0
	s_add_i32 s52, s0, s1
	s_ashr_i32 s1, s0, 31
	s_lshl_b64 s[0:1], s[0:1], 2
	v_readlane_b32 s12, v252, 25
	s_add_u32 s0, s12, s0
	v_readlane_b32 s12, v252, 26
	s_addc_u32 s1, s12, s1
	s_load_dword s12, s[0:1], 0x0 glc
	s_waitcnt lgkmcnt(0)
	v_readfirstlane_b32 s1, v2
	s_lshl_b32 s0, s12, 1
	s_or_b32 s53, s0, s1
